# attention loop: packed f32 VALU (v_pk_fma/add/mul_f32) split into scalar pairs (packed fp32 beside MFMAs stalls issue)
# speedup vs baseline: 1.0034x; 1.0034x over previous
; #define LAS __attribute__((address_space(3)))
;     ...
;             for (int ck = 0; ck < 4; ++ck) {
;                 if (!__any(qrel0 >= 64 * ck)) break;
;                 int qrel = qrel0; asm volatile("" : "+v"(qrel));
;                 bf16x8 ka[2][4];
; #pragma unroll
;                 for (int k2 = 0; k2 < 2; ++k2)
; #pragma unroll
;                     for (int kk = 0; kk < 4; ++kk) ka[k2][kk] = *(const LAS bf16x8*)(Ks + (32 * (2 * ck + k2) + qi) * KS_PITCH + (16 * kk + 8 * half) * 2);
;                 f32x16 sacc[2];
; #pragma unroll
;                 for (int k2 = 0; k2 < 2; ++k2) {
; #pragma unroll
;                     for (int i = 0; i < 16; ++i) sacc[k2][i] = 0.f;
; #pragma unroll
;                     for (int kk = 0; kk < 4; ++kk) sacc[k2] = __builtin_amdgcn_mfma_f32_32x32x16_bf16(ka[k2][kk], qf[kk], sacc[k2], 0, 0, 0); }
;                 float mx = -1e30f;
;                 if (__any(qrel <= 64 * ck + 191)) {
; #pragma unroll
;                     for (int k2 = 0; k2 < 2; ++k2) {
;                         float bb[16];
; #pragma unroll
;                         for (int i = 0; i < 16; ++i) { const int key = 32 * (2 * ck + k2) + (i & 3) + 8 * (i >> 2) + 4 * half; const int n = qrel - key;
;                             bb[i] = LUT[1 + (n < -1 ? -1 : (n > 128 ? 128 : n))]; }
; #pragma unroll
;                         for (int i = 0; i < 16; ++i) asm volatile("" : "+v"(bb[i]));
; #pragma unroll
;                         for (int i = 0; i < 16; ++i) { const float s = sacc[k2][i] + bb[i]; sacc[k2][i] = s; mx = fmaxf(mx, s); } }
;                 } else {
; #pragma unroll
;                     for (int k2 = 0; k2 < 2; ++k2)
; #pragma unroll
;                         for (int i = 0; i < 16; ++i) { const float s = sacc[k2][i] + bfar; sacc[k2][i] = s; mx = fmaxf(mx, s); }
;                 }
.LBB0_2230:
	v_mov_b32_e32 v64, v250
	s_waitcnt lgkmcnt(0)
	ds_read_b128 v[32:35], v251
	ds_read_b128 v[66:69], v251 offset:32
	ds_read_b128 v[70:73], v251 offset:64
	ds_read_b128 v[74:77], v251 offset:96
	ds_read_b128 v[78:81], v251 offset:4608
	ds_read_b128 v[122:125], v251 offset:4640
	v_cmp_ge_i32_e32 vcc, s22, v64
	s_waitcnt lgkmcnt(5)
	v_mfma_f32_32x32x16_bf16 v[48:63], v[32:35], v[110:113], 0
	s_waitcnt lgkmcnt(4)
	v_mfma_f32_32x32x16_bf16 v[48:63], v[66:69], v[106:109], v[48:63]
	ds_read_b128 v[66:69], v251 offset:4672
	s_waitcnt lgkmcnt(4)
	v_mfma_f32_32x32x16_bf16 v[48:63], v[70:73], v[102:105], v[48:63]
	ds_read_b128 v[70:73], v251 offset:4704
	s_waitcnt lgkmcnt(4)
	v_mfma_f32_32x32x16_bf16 v[48:63], v[74:77], v[98:101], v[48:63]
	s_waitcnt lgkmcnt(3)
	v_mfma_f32_32x32x16_bf16 v[32:47], v[78:81], v[110:113], 0
	s_waitcnt lgkmcnt(2)
	v_mfma_f32_32x32x16_bf16 v[32:47], v[122:125], v[106:109], v[32:47]
	s_waitcnt lgkmcnt(1)
	v_mfma_f32_32x32x16_bf16 v[32:47], v[66:69], v[102:105], v[32:47]
	s_waitcnt lgkmcnt(0)
	v_mfma_f32_32x32x16_bf16 v[32:47], v[70:73], v[98:101], v[32:47]
	s_cbranch_vccz .LBB0_2237
	v_add3_u32 v64, v155, v64, s21
	v_med3_i32 v235, v64, -1, s98
	v_lshl_add_u32 v235, v235, 2, s99
	ds_read_b32 v122, v235 offset:236
	ds_read_b32 v123, v235 offset:232
	ds_read_b32 v124, v235 offset:228
	ds_read_b32 v125, v235 offset:224
	ds_read_b32 v126, v235 offset:204
	ds_read_b32 v127, v235 offset:200
	ds_read_b32 v128, v235 offset:196
	ds_read_b32 v129, v235 offset:192
	ds_read_b32 v130, v235 offset:172
	ds_read_b32 v131, v235 offset:168
	ds_read_b32 v132, v235 offset:164
	ds_read_b32 v133, v235 offset:160
	ds_read_b32 v134, v235 offset:140
	ds_read_b32 v135, v235 offset:136
	ds_read_b32 v136, v235 offset:132
	ds_read_b32 v137, v235 offset:128
	s_waitcnt lgkmcnt(14)
	s_waitcnt lgkmcnt(13)
	s_waitcnt lgkmcnt(12)
	v_add_f32_e32 v122, v48, v122
	v_add_f32_e32 v123, v49, v123
	s_waitcnt lgkmcnt(11)
	s_waitcnt lgkmcnt(10)
	v_max3_f32 v138, v122, s23, v123
	v_add_f32_e32 v124, v50, v124
	v_add_f32_e32 v125, v51, v125
	s_waitcnt lgkmcnt(9)
	s_waitcnt lgkmcnt(8)
	v_max3_f32 v138, v138, v124, v125
	v_add_f32_e32 v126, v52, v126
	v_add_f32_e32 v127, v53, v127
	s_waitcnt lgkmcnt(7)
	s_waitcnt lgkmcnt(6)
	v_max3_f32 v138, v138, v126, v127
	v_add_f32_e32 v128, v54, v128
	v_add_f32_e32 v129, v55, v129
	s_waitcnt lgkmcnt(5)
	s_waitcnt lgkmcnt(4)
	v_max3_f32 v138, v138, v128, v129
	v_add_f32_e32 v130, v56, v130
	v_add_f32_e32 v131, v57, v131
	s_waitcnt lgkmcnt(3)
	s_waitcnt lgkmcnt(2)
	v_max3_f32 v138, v138, v130, v131
	v_add_f32_e32 v132, v58, v132
	v_add_f32_e32 v133, v59, v133
	s_waitcnt lgkmcnt(1)
	s_waitcnt lgkmcnt(0)
	v_max3_f32 v138, v138, v132, v133
	v_add_f32_e32 v134, v60, v134
	v_add_f32_e32 v135, v61, v135
	v_max3_f32 v138, v138, v134, v135
	v_add_f32_e32 v136, v62, v136
	v_add_f32_e32 v137, v63, v137
	v_max3_f32 v166, v138, v136, v137
	ds_read_b32 v138, v235 offset:108
	ds_read_b32 v139, v235 offset:104
	ds_read_b32 v140, v235 offset:100
	ds_read_b32 v141, v235 offset:96
	ds_read_b32 v168, v235 offset:76
	ds_read_b32 v169, v235 offset:72
	ds_read_b32 v170, v235 offset:68
	ds_read_b32 v171, v235 offset:64
	ds_read_b32 v172, v235 offset:44
	ds_read_b32 v173, v235 offset:40
	ds_read_b32 v174, v235 offset:36
	ds_read_b32 v175, v235 offset:32
	ds_read_b32 v204, v235 offset:12
	ds_read_b32 v205, v235 offset:8
	ds_read_b32 v226, v235 offset:4
	ds_read_b32 v227, v235 offset:0
	s_waitcnt lgkmcnt(14)
	s_waitcnt lgkmcnt(13)
	s_waitcnt lgkmcnt(12)
	s_waitcnt lgkmcnt(11)
	s_waitcnt lgkmcnt(10)
	s_waitcnt lgkmcnt(9)
	v_add_f32_e32 v164, v32, v138
	v_add_f32_e32 v165, v33, v139
	s_waitcnt lgkmcnt(8)
	v_add_f32_e32 v168, v36, v168
	v_add_f32_e32 v169, v37, v169
	v_max3_f32 v64, v166, v164, v165
	v_add_f32_e32 v166, v34, v140
	v_add_f32_e32 v167, v35, v141
	s_waitcnt lgkmcnt(7)
	s_waitcnt lgkmcnt(6)
	v_add_f32_e32 v170, v38, v170
	v_add_f32_e32 v171, v39, v171
	v_max3_f32 v64, v64, v166, v167
	v_max3_f32 v64, v64, v168, v169
	s_waitcnt lgkmcnt(5)
	s_waitcnt lgkmcnt(4)
	v_max3_f32 v64, v64, v170, v171
	v_add_f32_e32 v172, v40, v172
	v_add_f32_e32 v173, v41, v173
	v_add_f32_e32 v174, v42, v174
	v_add_f32_e32 v175, v43, v175
	v_max3_f32 v64, v64, v172, v173
	s_waitcnt lgkmcnt(3)
	s_waitcnt lgkmcnt(2)
	v_max3_f32 v64, v64, v174, v175
	v_add_f32_e32 v138, v44, v204
	v_add_f32_e32 v139, v45, v205
	s_waitcnt lgkmcnt(1)
	s_waitcnt lgkmcnt(0)
	v_max3_f32 v64, v64, v138, v139
	v_add_f32_e32 v140, v46, v226
	v_add_f32_e32 v141, v47, v227
	s_nop 0
	v_max3_f32 v64, v64, v140, v141
	s_cbranch_execnz .LBB0_2233
.LBB0_2232:
	v_add_f32_e32 v122, v114, v48
	v_add_f32_e32 v123, v115, v49
	v_add_f32_e32 v124, v114, v50
	v_add_f32_e32 v125, v115, v51
	v_max3_f32 v48, v122, s23, v123
	v_max3_f32 v48, v48, v124, v125
	v_add_f32_e32 v126, v114, v52
	v_add_f32_e32 v127, v115, v53
	v_add_f32_e32 v128, v114, v54
	v_add_f32_e32 v129, v115, v55
	v_max3_f32 v48, v48, v126, v127
	v_max3_f32 v48, v48, v128, v129
	v_add_f32_e32 v130, v114, v56
	v_add_f32_e32 v131, v115, v57
	v_add_f32_e32 v132, v114, v58
	v_add_f32_e32 v133, v115, v59
	v_max3_f32 v48, v48, v130, v131
	v_max3_f32 v48, v48, v132, v133
	v_add_f32_e32 v134, v114, v60
	v_add_f32_e32 v135, v115, v61
	v_add_f32_e32 v136, v114, v62
	v_add_f32_e32 v137, v115, v63
	v_max3_f32 v48, v48, v134, v135
	v_max3_f32 v48, v48, v136, v137
	v_add_f32_e32 v164, v114, v32
	v_add_f32_e32 v165, v115, v33
	v_add_f32_e32 v166, v114, v34
	v_add_f32_e32 v167, v115, v35
	v_max3_f32 v32, v48, v164, v165
	v_max3_f32 v32, v32, v166, v167
	v_add_f32_e32 v168, v114, v36
	v_add_f32_e32 v169, v115, v37
	v_add_f32_e32 v170, v114, v38
	v_add_f32_e32 v171, v115, v39
	v_max3_f32 v32, v32, v168, v169
	v_max3_f32 v32, v32, v170, v171
	v_add_f32_e32 v172, v114, v40
	v_add_f32_e32 v173, v115, v41
	v_add_f32_e32 v174, v114, v42
	v_add_f32_e32 v175, v115, v43
	v_max3_f32 v32, v32, v172, v173
	v_max3_f32 v32, v32, v174, v175
	v_add_f32_e32 v138, v114, v44
	v_add_f32_e32 v139, v115, v45
	v_add_f32_e32 v140, v114, v46
	v_add_f32_e32 v141, v115, v47
	v_max3_f32 v32, v32, v138, v139
	v_max3_f32 v64, v32, v140, v141

; #define LAS __attribute__((address_space(3)))
; DI unsigned pk2(float lo, float hi) { f32x2 v = {lo, hi}; return __builtin_bit_cast(unsigned, __builtin_convertvector(v, bf16v2)); }
;     ...
;                 mx = fmaxf(mx, __shfl_xor(mx, 32));
;                 const float mnew = fmaxf(mrun, mx); const bool grew = __any(mnew > mrun);
;                 if (grew) {
;                     const float alpha = __builtin_amdgcn_exp2f((mrun - mnew) * L2E);
;                     ls0 *= alpha; ls1 *= alpha; ls2 *= alpha; ls3 *= alpha;
; #pragma unroll
;                     for (int i = 0; i < 16; ++i) { oacc[0][i] *= alpha; oacc[1][i] *= alpha; } }
;                 mrun = mnew;
;                 const float nm = -mnew * L2E;
; #pragma unroll
;                 for (int k2 = 0; k2 < 2; ++k2) { const int kt = 2 * ck + k2;
; #pragma unroll
;                     for (int i = 0; i < 16; i += 4) { const float p0 = __builtin_amdgcn_exp2f(__builtin_fmaf(sacc[k2][i], L2E, nm)), p1 = __builtin_amdgcn_exp2f(__builtin_fmaf(sacc[k2][i + 1], L2E, nm)),
;                                                                   p2 = __builtin_amdgcn_exp2f(__builtin_fmaf(sacc[k2][i + 2], L2E, nm)), p3 = __builtin_amdgcn_exp2f(__builtin_fmaf(sacc[k2][i + 3], L2E, nm));
;                         sacc[k2][i] = p0; sacc[k2][i + 1] = p1; sacc[k2][i + 2] = p2; sacc[k2][i + 3] = p3; ls0 += p0; ls1 += p1; ls2 += p2; ls3 += p3; }
; #pragma unroll
;                     for (int cc = 0; cc < 2; ++cc) {
;                         u32x4 pw; pw.x = pk2(sacc[k2][8 * cc], sacc[k2][8 * cc + 1]); pw.y = pk2(sacc[k2][8 * cc + 2], sacc[k2][8 * cc + 3]); pw.z = pk2(sacc[k2][8 * cc + 4], sacc[k2][8 * cc + 5]); pw.w = pk2(sacc[k2][8 * cc + 6], sacc[k2][8 * cc + 7]);
;                         const bf16x8 pf = __builtin_bit_cast(bf16x8, pw);
;                         const int key0 = 32 * kt + 16 * cc + 4 * half;
; #pragma unroll
;                         for (int dt = 0; dt < 2; ++dt) { const LAS unsigned char* vb = Vt + (32 * dt + qi) * VT_PITCH + key0 * 2;
;                             const u32x2 va = *(const LAS u32x2*)vb, vb2 = *(const LAS u32x2*)(vb + 16);
;                             u32x4 vw; vw.x = va.x; vw.y = va.y; vw.z = vb2.x; vw.w = vb2.y;
;                             oacc[dt] = __builtin_amdgcn_mfma_f32_32x32x16_bf16(__builtin_bit_cast(bf16x8, vw), pf, oacc[dt], 0, 0, 0); } } }
;             }
.Lattn_resc:
	v_cndmask_b32_e32 v32, v202, v32, vcc
	v_sub_f32_e32 v33, v202, v32
	v_mul_f32_e32 v33, 0x3fb8aa3b, v33
	v_exp_f32_e32 v34, v33
	s_nop 0
	v_mul_f32_e32 v30, v34, v30
	v_mul_f32_e32 v31, v34, v31
	v_mul_f32_e32 v28, v34, v28
	v_mul_f32_e32 v29, v34, v29
	v_mul_f32_e32 v26, v34, v26
	v_mul_f32_e32 v27, v34, v27
	v_mul_f32_e32 v24, v34, v24
	v_mul_f32_e32 v25, v34, v25
	v_mul_f32_e32 v22, v34, v22
	v_mul_f32_e32 v23, v34, v23
	v_mul_f32_e32 v20, v34, v20
	v_mul_f32_e32 v21, v34, v21
	v_mul_f32_e32 v18, v34, v18
	v_mul_f32_e32 v19, v34, v19
	v_mul_f32_e32 v16, v34, v16
	v_mul_f32_e32 v17, v34, v17
	v_mul_f32_e32 v14, v34, v14
	v_mul_f32_e32 v15, v34, v15
	v_mul_f32_e32 v12, v34, v12
	v_mul_f32_e32 v13, v34, v13
	v_mul_f32_e32 v10, v34, v10
	v_mul_f32_e32 v11, v34, v11
	v_mul_f32_e32 v8, v34, v8
	v_mul_f32_e32 v9, v34, v9
	v_mul_f32_e32 v6, v34, v6
	v_mul_f32_e32 v7, v34, v7
	v_mul_f32_e32 v4, v34, v4
	v_mul_f32_e32 v5, v34, v5
	v_mul_f32_e32 v2, v34, v2
	v_mul_f32_e32 v3, v34, v3
	v_mul_f32_e32 v0, v34, v0
	v_mul_f32_e32 v1, v34, v1
	v_mul_f32_e32 v120, v34, v120
	v_mul_f32_e32 v121, v34, v121
	v_mul_f32_e32 v118, v34, v118
	v_mul_f32_e32 v119, v34, v119
.LBB0_2235:
	v_mul_f32_e32 v33, 0xbfb8aa3b, v32
	v_fmamk_f32 v126, v126, 0x3fb8aa3b, v33
	v_fmamk_f32 v127, v127, 0x3fb8aa3b, v33
	v_fmamk_f32 v122, v122, 0x3fb8aa3b, v33
	v_fmamk_f32 v123, v123, 0x3fb8aa3b, v33
	v_exp_f32_e32 v63, v126
	v_fmamk_f32 v128, v128, 0x3fb8aa3b, v33
	v_fmamk_f32 v129, v129, 0x3fb8aa3b, v33
	v_exp_f32_e32 v62, v127
	v_fmamk_f32 v124, v124, 0x3fb8aa3b, v33
	v_fmamk_f32 v125, v125, 0x3fb8aa3b, v33
	v_exp_f32_e32 v61, v122
	v_exp_f32_e32 v60, v123
	v_exp_f32_e32 v123, v128
	v_exp_f32_e32 v122, v129
	v_fmamk_f32 v130, v130, 0x3fb8aa3b, v33
	v_fmamk_f32 v131, v131, 0x3fb8aa3b, v33
	v_exp_f32_e32 v35, v124
	v_exp_f32_e32 v34, v125
	v_exp_f32_e32 v125, v130
	v_exp_f32_e32 v124, v131
	v_fmamk_f32 v132, v132, 0x3fb8aa3b, v33
	v_fmamk_f32 v133, v133, 0x3fb8aa3b, v33
	v_fmamk_f32 v164, v164, 0x3fb8aa3b, v33
	v_fmamk_f32 v165, v165, 0x3fb8aa3b, v33
	v_exp_f32_e32 v127, v132
	v_exp_f32_e32 v126, v133
	v_exp_f32_e32 v133, v164
	v_exp_f32_e32 v132, v165
	v_fmamk_f32 v134, v134, 0x3fb8aa3b, v33
	v_fmamk_f32 v135, v135, 0x3fb8aa3b, v33
	v_fmamk_f32 v166, v166, 0x3fb8aa3b, v33
	v_fmamk_f32 v167, v167, 0x3fb8aa3b, v33
	v_exp_f32_e32 v129, v134
	v_exp_f32_e32 v128, v135
	v_exp_f32_e32 v135, v166
	v_exp_f32_e32 v134, v167
	v_fmamk_f32 v136, v136, 0x3fb8aa3b, v33
	v_fmamk_f32 v137, v137, 0x3fb8aa3b, v33
	v_fmamk_f32 v168, v168, 0x3fb8aa3b, v33
	v_fmamk_f32 v169, v169, 0x3fb8aa3b, v33
	v_exp_f32_e32 v131, v136
	v_exp_f32_e32 v130, v137
	v_exp_f32_e32 v137, v168
	v_exp_f32_e32 v136, v169
	v_fmamk_f32 v170, v170, 0x3fb8aa3b, v33
	v_fmamk_f32 v171, v171, 0x3fb8aa3b, v33
	v_fmamk_f32 v172, v172, 0x3fb8aa3b, v33
	v_fmamk_f32 v173, v173, 0x3fb8aa3b, v33
	v_exp_f32_e32 v165, v170
	v_exp_f32_e32 v164, v171
	v_add_u32_e32 v58, 0x4000, v216
	v_exp_f32_e32 v167, v172
	v_exp_f32_e32 v166, v173
	v_fmamk_f32 v174, v174, 0x3fb8aa3b, v33
	v_fmamk_f32 v175, v175, 0x3fb8aa3b, v33
	ds_read2_b64 v[36:39], v216 offset1:2
	ds_read2_b64 v[40:43], v216 offset0:4 offset1:6
	ds_read2_b64 v[44:47], v58 offset0:32 offset1:34
	ds_read2_b64 v[48:51], v58 offset0:36 offset1:38
	v_fmamk_f32 v138, v138, 0x3fb8aa3b, v33
	v_fmamk_f32 v139, v139, 0x3fb8aa3b, v33
	v_exp_f32_e32 v169, v174
	v_exp_f32_e32 v168, v175
	v_cvt_pk_bf16_f32 v52, v61, v60
	v_cvt_pk_bf16_f32 v53, v35, v34
	v_cvt_pk_bf16_f32 v54, v63, v62
	v_cvt_pk_bf16_f32 v55, v123, v122
	v_exp_f32_e32 v171, v138
	v_exp_f32_e32 v170, v139
	s_waitcnt lgkmcnt(3)
	v_mfma_f32_32x32x16_bf16 v[16:31], v[36:39], v[52:55], v[16:31]
	v_fmamk_f32 v140, v140, 0x3fb8aa3b, v33
	v_fmamk_f32 v141, v141, 0x3fb8aa3b, v33
	v_cvt_pk_bf16_f32 v36, v125, v124
	v_exp_f32_e32 v139, v140
	s_waitcnt lgkmcnt(1)
	v_mfma_f32_32x32x16_bf16 v[0:15], v[44:47], v[52:55], v[0:15]
	v_cvt_pk_bf16_f32 v38, v129, v128
	v_cvt_pk_bf16_f32 v37, v127, v126
	v_add_f32_e32 v60, v60, v120
	v_add_f32_e32 v61, v61, v121
	v_cvt_pk_bf16_f32 v39, v131, v130
	v_exp_f32_e32 v138, v141
	s_nop 0
	v_mfma_f32_32x32x16_bf16 v[16:31], v[40:43], v[36:39], v[16:31]
	ds_read2_b64 v[40:43], v216 offset0:8 offset1:10
	ds_read2_b64 v[44:47], v58 offset0:40 offset1:42
	ds_read2_b64 v[52:55], v216 offset0:12 offset1:14
	ds_read2_b64 v[56:59], v58 offset0:44 offset1:46
	v_add_f32_e32 v34, v34, v118
	v_add_f32_e32 v35, v35, v119
	v_add_f32_e32 v34, v122, v34
	v_add_f32_e32 v35, v123, v35
	s_sub_i32 s21, s21, 64
	v_add_f32_e32 v34, v126, v34
	v_add_f32_e32 v35, v127, v35
	s_add_i32 s22, s22, 64
	s_waitcnt lgkmcnt(4)
	v_mfma_f32_32x32x16_bf16 v[0:15], v[48:51], v[36:39], v[0:15]
	v_cvt_pk_bf16_f32 v37, v135, v134
	v_cvt_pk_bf16_f32 v36, v133, v132
	v_cvt_pk_bf16_f32 v38, v137, v136
	v_cvt_pk_bf16_f32 v39, v165, v164
	v_add_f32_e32 v34, v130, v34
	v_add_f32_e32 v35, v131, v35
	s_cmpk_eq_i32 s21, 0xff00
	s_waitcnt lgkmcnt(3)
	v_mfma_f32_32x32x16_bf16 v[16:31], v[40:43], v[36:39], v[16:31]
	v_add_f32_e32 v40, v62, v60
	v_add_f32_e32 v41, v63, v61
	v_add_f32_e32 v40, v124, v40
	v_add_f32_e32 v41, v125, v41
	v_add_f32_e32 v34, v134, v34
	v_add_f32_e32 v35, v135, v35
	v_add_f32_e32 v40, v128, v40
	v_add_f32_e32 v41, v129, v41
	v_add_f32_e32 v34, v164, v34
	v_add_f32_e32 v35, v165, v35
	v_add_f32_e32 v40, v132, v40
	v_add_f32_e32 v41, v133, v41
	s_waitcnt lgkmcnt(2)
	v_mfma_f32_32x32x16_bf16 v[0:15], v[44:47], v[36:39], v[0:15]
	v_cvt_pk_bf16_f32 v36, v167, v166
	v_add_f32_e32 v40, v136, v40
	v_add_f32_e32 v41, v137, v41
	v_cvt_pk_bf16_f32 v37, v169, v168
	v_add_f32_e32 v40, v166, v40
	v_add_f32_e32 v41, v167, v41
	v_cvt_pk_bf16_f32 v38, v171, v170
	v_cvt_pk_bf16_f32 v39, v139, v138
	v_add_f32_e32 v34, v168, v34
	v_add_f32_e32 v35, v169, v35
	v_add_f32_e32 v120, v170, v40
	v_add_f32_e32 v121, v171, v41
	s_waitcnt lgkmcnt(1)
	v_mfma_f32_32x32x16_bf16 v[16:31], v[52:55], v[36:39], v[16:31]
	v_add_f32_e32 v118, v138, v34
	v_add_f32_e32 v119, v139, v35
	v_add_u32_e32 v216, 0x80, v216
	v_add_u32_e32 v251, 0x2400, v251
	s_cselect_b64 s[6:7], -1, 0
	s_waitcnt lgkmcnt(0)
	v_mfma_f32_32x32x16_bf16 v[0:15], v[56:59], v[36:39], v[0:15]
	s_and_b64 vcc, exec, s[6:7]
	s_cbranch_vccnz .LBB0_2238

; DI unsigned pk2(float lo, float hi) { f32x2 v = {lo, hi}; return __builtin_bit_cast(unsigned, __builtin_convertvector(v, bf16v2)); }
;     ...
;             float lsum = (ls0 + ls1) + (ls2 + ls3);
; #pragma unroll
;             for (int kk = 0; kk < 4; ++kk) asm volatile("" : "+v"(qfn[kk]));
;             asm volatile("" : "+v"(enn));
;             const float mx = mrun;
;             lsum += __shfl_xor(lsum, 32);
;             const float inv = 1.0f / lsum;
;             if (valid) {
;                 int hf = half; asm volatile("" : "+v"(hf));
;                 bf16_t* op = PO + ((size_t)slot * T + tok) * CW + h * 64 + 4 * hf;
; #pragma unroll
;                 for (int dt = 0; dt < 2; ++dt)
; #pragma unroll
;                     for (int ig = 0; ig < 4; ++ig) { u32x2 w; w.x = pk2(oacc[dt][4 * ig] * inv, oacc[dt][4 * ig + 1] * inv); w.y = pk2(oacc[dt][4 * ig + 2] * inv, oacc[dt][4 * ig + 3] * inv);
;                         *(u32x2*)(op + 32 * dt + 8 * ig) = w; }
;                 if (half == 0) PST[((size_t)slot * T + tok) * 8 + h] = (f32x2){mx, lsum};
;             }
.LBB0_2238:
	v_lshl_or_b32 v33, s20, 5, v149
	v_cmp_lt_i32_e32 vcc, v33, v245
	v_add_f32_e32 v33, v120, v121
	s_waitcnt lgkmcnt(0)
	v_add_f32_e32 v34, v118, v119
	v_add_f32_e32 v33, v34, v33
	s_nop 0
	v_mov_b32_e32 v34, v33
	s_nop 1
	v_permlane32_swap_b32_e32 v34, v33
	s_waitcnt vmcnt(3)
	s_waitcnt vmcnt(2)
	s_waitcnt vmcnt(1)
	s_waitcnt vmcnt(0)
	s_and_saveexec_b64 s[6:7], vcc
	s_cbranch_execz .LBB0_2225
	s_waitcnt lgkmcnt(0)
	v_add_f32_e32 v33, v33, v34
	v_div_scale_f32 v34, s[20:21], v33, v33, 1.0
	v_rcp_f32_e32 v35, v34
	v_div_scale_f32 v36, vcc, 1.0, v33, 1.0
	v_fma_f32 v37, -v34, v35, 1.0
	v_fmac_f32_e32 v35, v37, v35
	v_mul_f32_e32 v37, v36, v35
	v_fma_f32 v38, -v34, v37, v36
	v_fmac_f32_e32 v37, v38, v35
	v_fma_f32 v34, -v34, v37, v36
	v_mov_b32_e32 v36, 15
	v_lshlrev_b32_sdwa v36, v36, v248 dst_sel:DWORD dst_unused:UNUSED_PAD src0_sel:DWORD src1_sel:WORD_1
	v_div_fmas_f32 v34, v34, v35, v37
	v_mov_b32_e32 v35, v151
	v_add3_u32 v64, v249, s44, v36
	v_div_fixup_f32 v34, v34, v33, 1.0
	v_lshlrev_b64 v[36:37], 10, v[64:65]
	v_lshlrev_b32_e32 v38, 2, v35
	v_lshl_add_u64 v[36:37], s[0:1], 0, v[36:37]
	v_ashrrev_i32_e32 v39, 31, v38
	v_mul_f32_e32 v16, v34, v16
	v_mul_f32_e32 v17, v34, v17
	v_mul_f32_e32 v18, v34, v18
	v_mul_f32_e32 v19, v34, v19
	v_mul_f32_e32 v0, v34, v0
	v_mul_f32_e32 v1, v34, v1
	v_mul_f32_e32 v2, v34, v2
	v_mul_f32_e32 v3, v34, v3
	v_lshl_add_u64 v[36:37], v[38:39], 1, v[36:37]
	v_cvt_pk_bf16_f32 v16, v16, v17
	v_cvt_pk_bf16_f32 v17, v18, v19
	v_cvt_pk_bf16_f32 v0, v0, v1
	v_cvt_pk_bf16_f32 v1, v2, v3
	global_store_dwordx2 v[36:37], v[16:17], off
	v_mul_f32_e32 v16, v34, v20
	v_mul_f32_e32 v17, v34, v21
	v_mul_f32_e32 v18, v34, v22
	v_mul_f32_e32 v19, v34, v23
	global_store_dwordx2 v[36:37], v[0:1], off offset:64
	v_mul_f32_e32 v0, v34, v4
	v_mul_f32_e32 v1, v34, v5
	v_mul_f32_e32 v2, v34, v6
	v_mul_f32_e32 v3, v34, v7
	v_cvt_pk_bf16_f32 v16, v16, v17
	v_cvt_pk_bf16_f32 v17, v18, v19
	v_cvt_pk_bf16_f32 v0, v0, v1
	v_cvt_pk_bf16_f32 v1, v2, v3
	global_store_dwordx2 v[36:37], v[16:17], off offset:16
	v_mul_f32_e32 v16, v34, v24
	v_mul_f32_e32 v17, v34, v25
	v_mul_f32_e32 v18, v34, v26
	v_mul_f32_e32 v19, v34, v27
	global_store_dwordx2 v[36:37], v[0:1], off offset:80
	v_mul_f32_e32 v0, v34, v8
	v_mul_f32_e32 v1, v34, v9
	v_mul_f32_e32 v2, v34, v10
	v_mul_f32_e32 v3, v34, v11
	v_cvt_pk_bf16_f32 v16, v16, v17
	v_cvt_pk_bf16_f32 v17, v18, v19
	v_cvt_pk_bf16_f32 v0, v0, v1
	v_cvt_pk_bf16_f32 v1, v2, v3
	global_store_dwordx2 v[36:37], v[16:17], off offset:32
	v_mul_f32_e32 v16, v34, v28
	v_mul_f32_e32 v17, v34, v29
	v_mul_f32_e32 v18, v34, v30
	v_mul_f32_e32 v19, v34, v31
	global_store_dwordx2 v[36:37], v[0:1], off offset:96
	v_mul_f32_e32 v0, v34, v12
	v_mul_f32_e32 v1, v34, v13
	v_mul_f32_e32 v2, v34, v14
	v_mul_f32_e32 v3, v34, v15
	v_cvt_pk_bf16_f32 v16, v16, v17
	v_cvt_pk_bf16_f32 v17, v18, v19
	v_cvt_pk_bf16_f32 v0, v0, v1
	v_cvt_pk_bf16_f32 v1, v2, v3
	global_store_dwordx2 v[36:37], v[16:17], off offset:48
	global_store_dwordx2 v[36:37], v[0:1], off offset:112
	s_and_b64 exec, exec, s[12:13]
	s_cbranch_execz .LBB0_2225
	v_lshlrev_b64 v[0:1], 6, v[64:65]
	v_lshl_add_u64 v[0:1], s[2:3], 0, v[0:1]
	global_store_dwordx2 v[0:1], v[32:33], off
	s_branch .LBB0_2225
